# unit heads: division by the group size min(nM-fm,8) (always 8 for these shapes) replaced by a shift; on top of snake order + de-serialised rs fill + slimmed load segments
# baseline (speedup 1.0000x reference)
;     __device__ bool next(int i, Unit& u) const { const int rounds = nwg / G; if (i >= rounds) return false; return StaticOrder::next(rounds - 1 - i, u); }
;     __device__ bool next(int i, Unit& u) const { const int rounds = nwg / G; if (i >= 2 * rounds) return false; const bool ok = StaticOrder::next(i >= rounds ? i - rounds : i, u); u.z = (i >= rounds) ? 1 : 0; return ok; }
;     __host__ __device__ bool next(int i, Unit& u) const {
;         const long L = (long)i * G + c; if (L >= nwg) return false;
;         int wgid = (int)L; { const int q = nwg / NXCD, r = nwg % NXCD, xcd = wgid % NXCD, off = wgid / NXCD; wgid = (xcd < r ? xcd * (q + 1) : r * (q + 1) + (xcd - r) * q) + off; }
;         const int nig = WGM * nN, gid = wgid / nig, fm = gid * WGM, gsz = (nM - fm) < WGM ? (nM - fm) : WGM;
;         u.pm = fm + ((wgid % nig) % gsz); u.pn = (wgid % nig) / gsz; u.z = 0; return true;
.LBB0_125:
	v_readlane_b32 s8, v252, 10
	s_add_i32 s42, s42, 1
	v_readlane_b32 s9, v252, 11
	s_mul_i32 s4, s42, s9
	s_mul_hi_u32 s5, s42, s8
	s_add_i32 s5, s5, s4
	s_mul_i32 s4, s42, s8
	v_readlane_b32 s8, v252, 54
	v_readlane_b32 s9, v252, 55
	s_add_u32 s4, s4, s8
	s_addc_u32 s5, s5, s9
	v_mov_b64_e32 v[4:5], 0x1600
	v_cmp_lt_i64_e64 s[10:11], s[4:5], v[4:5]
	v_mov_b64_e32 v[4:5], 0x15ff
	v_cmp_gt_i64_e32 vcc, s[4:5], v[4:5]
	s_cbranch_vccnz .LBB0_127
	s_ashr_i32 s5, s4, 31
	s_lshr_b32 s5, s5, 29
	s_add_i32 s5, s4, s5
	s_ashr_i32 s8, s5, 3
	s_and_b32 s5, s5, -8
	s_sub_i32 s4, s4, s5
	s_cmp_lt_i32 s4, 0
	s_movk_i32 s5, 0x2c1
	s_cselect_b32 s5, s5, 0x2c0
	s_mul_i32 s4, s4, s5
	s_add_i32 s4, s4, s8
	s_mul_hi_i32 s5, s4, 0x2e8ba2e9
	s_lshr_b32 s8, s5, 31
	s_ashr_i32 s5, s5, 6
	s_add_i32 s5, s5, s8
	s_lshl_b32 s8, s5, 3
	s_sub_i32 s9, 0x80, s8
	s_min_i32 s9, s9, 8
	s_abs_i32 s22, s9
	s_mulk_i32 s5, 0x160
	s_sub_i32 s4, s4, s5
	s_ashr_i32 s22, s4, 3
	s_mul_i32 s5, s22, s9
	s_sub_i32 s4, s4, s5
	s_add_i32 s44, s8, s4

;     __device__ bool next(int i, Unit& u) const { const int rounds = nwg / G; if (i >= rounds) return false; return StaticOrder::next(rounds - 1 - i, u); }
;     __device__ bool next(int i, Unit& u) const { const int rounds = nwg / G; if (i >= 2 * rounds) return false; const bool ok = StaticOrder::next(i >= rounds ? i - rounds : i, u); u.z = (i >= rounds) ? 1 : 0; return ok; }
;     __host__ __device__ bool next(int i, Unit& u) const {
;         const long L = (long)i * G + c; if (L >= nwg) return false;
;         int wgid = (int)L; { const int q = nwg / NXCD, r = nwg % NXCD, xcd = wgid % NXCD, off = wgid / NXCD; wgid = (xcd < r ? xcd * (q + 1) : r * (q + 1) + (xcd - r) * q) + off; }
;         const int nig = WGM * nN, gid = wgid / nig, fm = gid * WGM, gsz = (nM - fm) < WGM ? (nM - fm) : WGM;
;         u.pm = fm + ((wgid % nig) % gsz); u.pn = (wgid % nig) / gsz; u.z = 0; return true;
.LBB0_213:
	v_readlane_b32 s2, v254, 46
	s_add_i32 s0, s0, s2
	s_ashr_i32 s2, s0, 31
	s_lshr_b32 s2, s2, 26
	s_add_i32 s2, s0, s2
	s_ashr_i32 s3, s2, 6
	s_lshl_b32 s3, s3, 3
	s_sub_i32 s4, 0x80, s3
	s_min_i32 s4, s4, 8
	s_abs_i32 s5, s4
	s_andn2_b32 s2, s2, 63
	s_sub_i32 s0, s0, s2
	s_ashr_i32 s2, s0, 3
	s_mul_i32 s4, s2, s4
	s_sub_i32 s0, s0, s4
	s_add_i32 s3, s3, s0
	s_mov_b64 s[4:5], -1

;     __host__ __device__ bool next(int i, Unit& u) const {
;     ...
;         int wgid = (int)L; { const int q = nwg / NXCD, r = nwg % NXCD, xcd = wgid % NXCD, off = wgid / NXCD; wgid = (xcd < r ? xcd * (q + 1) : r * (q + 1) + (xcd - r) * q) + off; }
;         const int nig = WGM * nN, gid = wgid / nig, fm = gid * WGM, gsz = (nM - fm) < WGM ? (nM - fm) : WGM;
;         u.pm = fm + ((wgid % nig) % gsz); u.pn = (wgid % nig) / gsz; u.z = 0; return true;
.LBB0_227:
	s_ashr_i32 s0, s0, 3
	s_add_i32 s0, s9, s0
	s_ashr_i32 s4, s0, 31
	s_lshr_b32 s4, s4, 26
	s_add_i32 s4, s0, s4
	s_ashr_i32 s5, s4, 6
	s_lshl_b32 s5, s5, 3
	s_sub_i32 s8, 0x80, s5
	s_min_i32 s8, s8, 8
	s_abs_i32 s9, s8
	s_andn2_b32 s4, s4, 63
	s_sub_i32 s0, s0, s4
	s_ashr_i32 s40, s0, 3
	s_mul_i32 s4, s40, s8
	s_sub_i32 s0, s0, s4
	s_add_i32 s41, s5, s0
	s_mov_b64 s[4:5], -1

;     __host__ __device__ bool next(int i, Unit& u) const {
;     ...
;         int wgid = (int)L; { const int q = nwg / NXCD, r = nwg % NXCD, xcd = wgid % NXCD, off = wgid / NXCD; wgid = (xcd < r ? xcd * (q + 1) : r * (q + 1) + (xcd - r) * q) + off; }
;         const int nig = WGM * nN, gid = wgid / nig, fm = gid * WGM, gsz = (nM - fm) < WGM ? (nM - fm) : WGM;
;         u.pm = fm + ((wgid % nig) % gsz); u.pn = (wgid % nig) / gsz; u.z = 0; return true;
.LBB0_320:
	s_ashr_i32 s3, s3, 3
	s_add_i32 s3, s9, s3
	s_ashr_i32 s4, s3, 31
	s_lshr_b32 s4, s4, 23
	s_add_i32 s4, s3, s4
	s_ashr_i32 s5, s4, 9
	s_lshl_b32 s5, s5, 3
	s_sub_i32 s8, 0x80, s5
	s_min_i32 s8, s8, 8
	s_abs_i32 s9, s8
	s_and_b32 s4, s4, 0xfffffe00
	s_sub_i32 s3, s3, s4
	s_ashr_i32 s22, s3, 3
	s_mul_i32 s4, s22, s8
	s_sub_i32 s3, s3, s4
	s_add_i32 s42, s5, s3

;     __host__ __device__ bool next(int i, Unit& u) const {
;     ...
;         int wgid = (int)L; { const int q = nwg / NXCD, r = nwg % NXCD, xcd = wgid % NXCD, off = wgid / NXCD; wgid = (xcd < r ? xcd * (q + 1) : r * (q + 1) + (xcd - r) * q) + off; }
;         const int nig = WGM * nN, gid = wgid / nig, fm = gid * WGM, gsz = (nM - fm) < WGM ? (nM - fm) : WGM;
;         u.pm = fm + ((wgid % nig) % gsz); u.pn = (wgid % nig) / gsz; u.z = 0; return true;
.LBB0_589:
	s_ashr_i32 s3, s3, 3
	s_add_i32 s3, s17, s3
	s_ashr_i32 s14, s3, 31
	s_lshr_b32 s14, s14, 26
	s_add_i32 s14, s3, s14
	s_ashr_i32 s15, s14, 6
	s_lshl_b32 s15, s15, 3
	s_sub_i32 s16, 0x80, s15
	s_min_i32 s16, s16, 8
	s_abs_i32 s17, s16
	s_andn2_b32 s14, s14, 63
	s_sub_i32 s3, s3, s14
	s_ashr_i32 s14, s3, 3
	s_mul_i32 s16, s14, s16
	s_sub_i32 s3, s3, s16
	s_add_i32 s3, s15, s3

;     __host__ __device__ bool next(int i, Unit& u) const {
;     ...
;         int wgid = (int)L; { const int q = nwg / NXCD, r = nwg % NXCD, xcd = wgid % NXCD, off = wgid / NXCD; wgid = (xcd < r ? xcd * (q + 1) : r * (q + 1) + (xcd - r) * q) + off; }
;         const int nig = WGM * nN, gid = wgid / nig, fm = gid * WGM, gsz = (nM - fm) < WGM ? (nM - fm) : WGM;
;         u.pm = fm + ((wgid % nig) % gsz); u.pn = (wgid % nig) / gsz; u.z = 0; return true;
.LBB0_696:
	s_ashr_i32 s3, s3, 3
	s_add_i32 s3, s9, s3
	s_ashr_i32 s4, s3, 31
	s_lshr_b32 s4, s4, 26
	s_add_i32 s4, s3, s4
	s_ashr_i32 s5, s4, 6
	s_lshl_b32 s5, s5, 3
	s_sub_i32 s8, 0x80, s5
	s_min_i32 s8, s8, 8
	s_abs_i32 s9, s8
	s_andn2_b32 s4, s4, 63
	s_sub_i32 s3, s3, s4
	s_ashr_i32 s18, s3, 3
	s_mul_i32 s4, s18, s8
	s_sub_i32 s3, s3, s4
	s_add_i32 s39, s5, s3
